# attention: per-XCD conversion stagger restored (kx = ((blockIdx&7)*3)>>3) now that instance 1 also has the QK^T read-ahead; conversion streams overlap other XCDs' attention
# speedup vs baseline: 1.0097x; 1.0015x over previous
.LBB0_2667:
	ds_read_b128 v[4:7], v207 offset:49152
	ds_read_b128 v[8:11], v207 offset:57344
	ds_read_b128 v[12:15], v208 offset:49152
	ds_read_b128 v[20:23], v208 offset:57344
	ds_read_b128 v[24:27], v209 offset:49152
	ds_read_b128 v[28:31], v209 offset:57344
	ds_read_b128 v[228:231], v210 offset:49152
	ds_read_b128 v[232:235], v210 offset:57344
	ds_read_b128 v[238:241], v207 offset:49280
	ds_read_b128 v[242:245], v191 offset:4096
	s_waitcnt lgkmcnt(9)
	v_mfma_f32_32x32x16_bf16 v[114:129], v[4:7], v[174:177], 0
	ds_read_b128 v[4:7], v207 offset:57472
	s_waitcnt lgkmcnt(9)
	v_mfma_f32_32x32x16_bf16 v[98:113], v[8:11], v[174:177], 0
	ds_read_b128 v[8:11], v208 offset:49280
	s_waitcnt lgkmcnt(9)
	v_mfma_f32_32x32x16_bf16 v[114:129], v[12:15], v[170:173], v[114:129]
	ds_read_b128 v[12:15], v191 offset:5120
	s_waitcnt lgkmcnt(9)
	v_mfma_f32_32x32x16_bf16 v[98:113], v[20:23], v[170:173], v[98:113]
	ds_read_b128 v[20:23], v208 offset:57472
	s_waitcnt lgkmcnt(9)
	v_mfma_f32_32x32x16_bf16 v[114:129], v[24:27], v[166:169], v[114:129]
	ds_read_b128 v[24:27], v209 offset:49280
	s_waitcnt lgkmcnt(9)
	v_mfma_f32_32x32x16_bf16 v[98:113], v[28:31], v[166:169], v[98:113]
	ds_read_b128 v[28:31], v191 offset:6144
	s_waitcnt lgkmcnt(9)
	v_mfma_f32_32x32x16_bf16 v[114:129], v[228:231], v[162:165], v[114:129]
	ds_read_b128 v[228:231], v209 offset:57472
	s_waitcnt lgkmcnt(9)
	v_mfma_f32_32x32x16_bf16 v[98:113], v[232:235], v[162:165], v[98:113]
	ds_read_b128 v[232:235], v210 offset:49280
	s_waitcnt lgkmcnt(8)
	v_mfma_f32_32x32x16_bf16 v[114:129], v[238:241], v[242:245], v[114:129]
	ds_read_b128 v[238:241], v191 offset:7168
	s_waitcnt lgkmcnt(8)
	v_mfma_f32_32x32x16_bf16 v[98:113], v[4:7], v[242:245], v[98:113]
	ds_read_b128 v[4:7], v210 offset:57472
	s_waitcnt lgkmcnt(7)
	v_mfma_f32_32x32x16_bf16 v[114:129], v[8:11], v[12:15], v[114:129]
	s_waitcnt lgkmcnt(6)
	v_mfma_f32_32x32x16_bf16 v[98:113], v[20:23], v[12:15], v[98:113]
	s_waitcnt lgkmcnt(4)
	v_mfma_f32_32x32x16_bf16 v[114:129], v[24:27], v[28:31], v[114:129]
	s_waitcnt lgkmcnt(3)
	v_mfma_f32_32x32x16_bf16 v[98:113], v[228:231], v[28:31], v[98:113]
	s_waitcnt lgkmcnt(1)
	v_mfma_f32_32x32x16_bf16 v[114:129], v[232:235], v[238:241], v[114:129]
	s_waitcnt lgkmcnt(0)
	v_mfma_f32_32x32x16_bf16 v[98:113], v[4:7], v[238:241], v[98:113]
	s_branch .LBB0_2671

.LBB0_2697:
	ds_read_b128 v[20:23], v207 offset:32768
	ds_read_b128 v[24:27], v207 offset:40960
	ds_read_b128 v[28:31], v208 offset:32768
	ds_read_b128 v[228:231], v208 offset:40960
	ds_read_b128 v[232:235], v209 offset:32768
	ds_read_b128 v[238:241], v209 offset:40960
	ds_read_b128 v[242:245], v210 offset:32768
	ds_read_b128 v[250:253], v210 offset:40960
	s_waitcnt lgkmcnt(7)
	v_mfma_f32_32x32x16_bf16 v[114:129], v[20:23], v[174:177], 0
	ds_read_b128 v[20:23], v207 offset:32896
	s_waitcnt lgkmcnt(7)
	v_mfma_f32_32x32x16_bf16 v[98:113], v[24:27], v[174:177], 0
	ds_read_b128 v[24:27], v191 offset:4096
	s_waitcnt lgkmcnt(7)
	v_mfma_f32_32x32x16_bf16 v[114:129], v[28:31], v[170:173], v[114:129]
	ds_read_b128 v[28:31], v207 offset:41088
	s_waitcnt lgkmcnt(7)
	v_mfma_f32_32x32x16_bf16 v[98:113], v[228:231], v[170:173], v[98:113]
	ds_read_b128 v[228:231], v208 offset:32896
	s_waitcnt lgkmcnt(7)
	v_mfma_f32_32x32x16_bf16 v[114:129], v[232:235], v[166:169], v[114:129]
	ds_read_b128 v[232:235], v191 offset:5120
	s_waitcnt lgkmcnt(7)
	v_mfma_f32_32x32x16_bf16 v[98:113], v[238:241], v[166:169], v[98:113]
	ds_read_b128 v[238:241], v208 offset:41088
	s_waitcnt lgkmcnt(7)
	v_mfma_f32_32x32x16_bf16 v[114:129], v[242:245], v[162:165], v[114:129]
	ds_read_b128 v[242:245], v209 offset:32896
	s_waitcnt lgkmcnt(7)
	v_mfma_f32_32x32x16_bf16 v[98:113], v[250:253], v[162:165], v[98:113]
	ds_read_b128 v[250:253], v191 offset:6144
	s_waitcnt lgkmcnt(6)
	v_mfma_f32_32x32x16_bf16 v[114:129], v[20:23], v[24:27], v[114:129]
	ds_read_b128 v[20:23], v209 offset:41088
	s_waitcnt lgkmcnt(6)
	v_mfma_f32_32x32x16_bf16 v[98:113], v[28:31], v[24:27], v[98:113]
	ds_read_b128 v[28:31], v210 offset:32896
	ds_read_b128 v[24:27], v191 offset:7168
	s_waitcnt lgkmcnt(6)
	v_mfma_f32_32x32x16_bf16 v[114:129], v[228:231], v[232:235], v[114:129]
	ds_read_b128 v[228:231], v210 offset:41088
	s_waitcnt lgkmcnt(6)
	v_mfma_f32_32x32x16_bf16 v[98:113], v[238:241], v[232:235], v[98:113]
	s_waitcnt lgkmcnt(4)
	v_mfma_f32_32x32x16_bf16 v[114:129], v[242:245], v[250:253], v[114:129]
	s_waitcnt lgkmcnt(3)
	v_mfma_f32_32x32x16_bf16 v[98:113], v[20:23], v[250:253], v[98:113]
	s_waitcnt lgkmcnt(1)
	v_mfma_f32_32x32x16_bf16 v[114:129], v[28:31], v[24:27], v[114:129]
	s_waitcnt lgkmcnt(0)
	v_mfma_f32_32x32x16_bf16 v[98:113], v[228:231], v[24:27], v[98:113]
	s_branch .LBB0_2701
